# P2 rebalance: the one VW precompute unit of each chain workgroup moves to the gMLP workgroups (4 instead of 3)
# baseline (speedup 1.0000x reference)
; __global__ void __launch_bounds__(NTHREADS, 2) fwd_kernel(Args args) {
;     ...
;         const bool split = (F.G == 256), chainwg = split && F.c < 128; const int jw = F.c & 127;
;         { PreOrder<0> S{split ? jw : F.c, split ? 128 : F.G, split ? (chainwg ? 0 : 4) : 512, (const char*)ws}; EpiPre<0> E{(unsigned char*)args.out};
;           pg8::gemm_phase<EpiPre<0>, PreOrder<0>>(F.lds + RING_OFF, F.lds + LDS_G_OFF, 4096, 2048, 4, S, E, 0); }
;         { PreOrder<1> S{split ? (chainwg ? 384 + jw : jw) : F.c, split ? 128 : F.G, split ? (chainwg ? 1 : 3) : 512, (const char*)ws}; EpiPre<1> E{(unsigned char*)args.out + (size_t)BATCH * 1024 * 1024};
;           pg8::gemm_phase<EpiPre<1>, PreOrder<1>>(F.lds + RING_OFF, F.lds + LDS_G_OFF, 2048, 4096, 4, S, E, 0); }
.LBB0_460:
	s_or_b32 s6, s27, 0x200
	s_and_b64 s[2:3], s[4:5], exec
	s_cselect_b32 s6, s6, s27
	s_and_b64 s[2:3], exec, s[8:9]
	s_cselect_b32 s46, s6, s33
	v_mov_b32_e32 v135, v0
	s_cmpk_gt_i32 s46, 0x1ff
	s_nop 0
	v_readfirstlane_b32 s13, v135
	s_cbranch_scc1 .LBB0_481
	s_and_b64 s[2:3], s[4:5], exec
	s_cselect_b32 s4, 1, 4
	s_and_b64 s[2:3], exec, s[8:9]
	s_cselect_b32 s47, s4, 0x200
	s_ashr_i32 s4, s46, 4
	s_bfe_u32 s60, s46, 0x20002
	s_and_b32 s49, s46, 3
	s_add_u32 s48, s58, 0xe00000
	s_addc_u32 s51, s59, 0
	s_lshl_b32 s2, s49, 19
	s_add_u32 s2, s48, s2
	s_addc_u32 s3, s51, 0
	s_lshl_b32 s8, s60, 9
	s_add_u32 s6, s2, s8
	s_addc_u32 s7, s3, 0
	s_ashr_i32 s5, s4, 31
	s_lshl_b64 s[2:3], s[4:5], 20
	s_add_u32 s2, s58, s2
	s_addc_u32 s3, s59, s3
	s_add_u32 s2, s2, s8
	s_addc_u32 s3, s3, 0
	s_add_u32 s8, s2, 0x25000800
	s_addc_u32 s9, s3, 0
	s_cmp_gt_u32 s47, 1
	s_cselect_b64 s[2:3], -1, 0
	s_add_i32 s11, s50, s46
	s_cmpk_lt_i32 s11, 0x200
	s_cselect_b64 s[14:15], -1, 0
	s_and_b64 s[14:15], s[2:3], s[14:15]
	s_ashr_i32 s10, s11, 4
	s_bfe_u32 s5, s11, 0x20002
	s_and_b32 s12, s11, 3
	s_andn2_b64 vcc, exec, s[14:15]
	s_mov_b64 s[24:25], s[8:9]
	s_mov_b64 s[2:3], s[6:7]
	s_cbranch_vccnz .LBB0_463
	s_lshl_b32 s2, s12, 19
	s_add_u32 s2, s48, s2
	s_addc_u32 s3, s51, 0
	s_lshl_b32 s20, s5, 9
	s_add_u32 s2, s2, s20
	s_addc_u32 s3, s3, 0
	s_ashr_i32 s11, s10, 31
	s_lshl_b64 s[18:19], s[10:11], 20
	s_add_u32 s11, s58, s18
	s_addc_u32 s18, s59, s19
	s_add_u32 s11, s11, s20
	s_addc_u32 s18, s18, 0
	s_add_u32 s24, s11, 0x25000800
	s_addc_u32 s25, s18, 0
